# MLA: last 8 exp2 of each tile deferred to the next step head (behind the K-fragment reads); SB self-max removed; barrier XGEN before leader inv
# baseline (speedup 1.0000x reference)
; #define LAS __attribute__((address_space(3)))
; __device__ __forceinline__ float ex2(float x) { return __builtin_amdgcn_exp2f(x); }
; __device__ __forceinline__ float lg2(float x) { return __builtin_amdgcn_logf(x); }
; __device__ __forceinline__ f32x16 mfma32(bf16x8 a, bf16x8 b, f32x16 c) { return __builtin_amdgcn_mfma_f32_32x32x16_bf16(a, b, c, 0, 0, 0); }
; #define SB_DMA(t, s) do { glds(ksrc + (size_t)(t) * 64 * INP, shm + (s) * KS_SB + wid * 1024); glds(vsrc + (size_t)(t) * 64 * INP, shm + SB_VOFF + (s) * VS + wid * 1024); } while (0)
; __device__ __forceinline__ void sb_unit(int b, int h, int qb, const bf16_t* __restrict__ PROJ, bf16_t* OCAT, float* SSQO, ldsp shm, volatile LAS unsigned* FL) {
;     ...
;         SB_DMA(SB_TILE(step + 3), (step + 3) & 3);
;         if (t <= tdw && !wfin) {
;             const LAS unsigned char* kb = shm + (step & 3) * KS_SB + hi * 1024 + r32 * 16;
;             f32x16 z0 = f32x16{}, z1 = f32x16{};
; #pragma unroll
;             for (int d0 = 0; d0 < 4; ++d0) { const bf16x8 k0 = *(const LAS bf16x8*)(kb + d0 * 2048), k1 = *(const LAS bf16x8*)(kb + d0 * 2048 + 512);
;                 z0 = mfma32(k0, qr[d0], z0); z1 = mfma32(k1, qr[d0], z1); }
;             const bool diag = (t == tdw); const int kb0 = t * 64 + 4 * hi;
;             f32x16 l0, l1; float tot = 0.f;
; #pragma unroll
;             for (int r = 0; r < 16; ++r) { l0[r] = -lg2(1.0f + ex2(fminf(z0[r], 100.f))); l1[r] = -lg2(1.0f + ex2(fminf(z1[r], 100.f))); }
.LBB0_1055:
	s_or_b64 exec, exec, s[4:5]
	s_add_i32 s6, s34, s2
	s_max_i32 s8, s6, 0
	s_add_i32 s7, s3, 0x6000
	s_lshl_b64 s[4:5], s[8:9], 18
	s_and_b32 s7, s7, 0x6000
	v_lshl_add_u64 v[38:39], v[154:155], 0, s[4:5]
	s_add_i32 s7, s26, s7
	v_lshl_add_u64 v[38:39], v[38:39], 0, s[82:83]
	s_mov_b32 m0, s7
	s_add_i32 s6, s6, 3
	global_load_lds_dwordx4 v[38:39], off
	v_lshl_add_u64 v[38:39], v[156:157], 0, s[4:5]
	v_lshl_add_u64 v[38:39], v[38:39], 0, s[84:85]
	s_add_i32 m0, s7, 0x8000
	s_cmp_gt_i32 s6, s35
	global_load_lds_dwordx4 v[38:39], off
	s_cselect_b64 s[4:5], -1, 0
	s_or_b64 s[4:5], s[0:1], s[4:5]
	s_and_b64 vcc, exec, s[4:5]
	s_cbranch_vccnz .LBB0_1061
	s_and_b32 s8, s3, 0x6000
	v_add_u32_e32 v1, s8, v164
	ds_read_b128 v[38:41], v1
	ds_read_b128 v[42:45], v1 offset:512
	s_cmp_eq_u32 s27, s2
	s_cselect_b64 s[16:17], -1, 0
	s_cmp_lg_u32 s27, s2
	s_waitcnt lgkmcnt(0)
	v_mfma_f32_32x32x16_bf16 v[98:113], v[38:41], v[130:133], 0
	v_mfma_f32_32x32x16_bf16 v[82:97], v[42:45], v[130:133], 0
	ds_read_b128 v[38:41], v1 offset:2048
	ds_read_b128 v[42:45], v1 offset:2560
	s_waitcnt lgkmcnt(0)
	v_mfma_f32_32x32x16_bf16 v[82:97], v[42:45], v[134:137], v[82:97]
	v_mfma_f32_32x32x16_bf16 v[98:113], v[38:41], v[134:137], v[98:113]
	ds_read_b128 v[38:41], v1 offset:4096
	ds_read_b128 v[42:45], v1 offset:4608
	s_waitcnt lgkmcnt(0)
	v_mfma_f32_32x32x16_bf16 v[82:97], v[42:45], v[138:141], v[82:97]
	v_mfma_f32_32x32x16_bf16 v[98:113], v[38:41], v[138:141], v[98:113]
	ds_read_b128 v[38:41], v1 offset:6144
	ds_read_b128 v[42:45], v1 offset:6656
	s_waitcnt lgkmcnt(0)
	v_mfma_f32_32x32x16_bf16 v[82:97], v[42:45], v[142:145], v[82:97]
	v_mfma_f32_32x32x16_bf16 v[98:113], v[38:41], v[142:145], v[98:113]
	s_nop 10
	v_min_f32_e32 v2, 0x42c80000, v82
	v_exp_f32_e32 v2, v2
	v_min_f32_e32 v60, 0x42c80000, v94
	v_exp_f32_e32 v60, v60
	v_add_f32_e32 v2, 1.0, v2
	v_min_f32_e32 v37, 0x42c80000, v99
	v_exp_f32_e32 v37, v37
	v_min_f32_e32 v1, 0x42c80000, v98
	v_exp_f32_e32 v1, v1
	v_log_f32_e32 v38, v2
	v_add_f32_e32 v2, 1.0, v37
	v_log_f32_e32 v37, v2
	v_add_f32_e32 v1, 1.0, v1
	v_min_f32_e32 v2, 0x42c80000, v83
	v_log_f32_e32 v1, v1
	v_exp_f32_e32 v39, v2
	v_xor_b32_e32 v52, 0x80000000, v38
	v_xor_b32_e32 v2, 0x80000000, v1
	v_xor_b32_e32 v1, 0x80000000, v37
	v_add_f32_e32 v37, 1.0, v39
	v_min_f32_e32 v38, 0x42c80000, v100
	v_min_f32_e32 v39, 0x42c80000, v84
	v_exp_f32_e32 v38, v38
	v_exp_f32_e32 v39, v39
	v_min_f32_e32 v59, 0x42c80000, v110
	v_exp_f32_e32 v59, v59
	v_add_f32_e32 v38, 1.0, v38
	v_add_f32_e32 v39, 1.0, v39
	v_log_f32_e32 v38, v38
	v_log_f32_e32 v39, v39
	v_add_f32_e32 v59, 1.0, v59
	v_log_f32_e32 v74, v59
	v_add_f32_e32 v59, 1.0, v60
	v_min_f32_e32 v60, 0x42c80000, v111
	v_min_f32_e32 v40, 0x42c80000, v101
	v_xor_b32_e32 v54, 0x80000000, v38
	v_xor_b32_e32 v56, 0x80000000, v39
	v_exp_f32_e32 v60, v60
	v_min_f32_e32 v61, 0x42c80000, v95
	v_log_f32_e32 v37, v37
	v_exp_f32_e32 v40, v40
	v_min_f32_e32 v38, 0x42c80000, v85
	v_min_f32_e32 v39, 0x42c80000, v102
	v_exp_f32_e32 v61, v61
	v_exp_f32_e32 v38, v38
	v_exp_f32_e32 v39, v39
	v_log_f32_e32 v75, v59
	v_add_f32_e32 v59, 1.0, v60
	v_xor_b32_e32 v53, 0x80000000, v37
	v_add_f32_e32 v37, 1.0, v40
	v_log_f32_e32 v77, v59
	v_add_f32_e32 v59, 1.0, v61
	v_min_f32_e32 v60, 0x42c80000, v112
	v_add_f32_e32 v38, 1.0, v38
	v_add_f32_e32 v39, 1.0, v39
	v_min_f32_e32 v40, 0x42c80000, v86
	v_exp_f32_e32 v60, v60
	v_min_f32_e32 v61, 0x42c80000, v96
	v_log_f32_e32 v37, v37
	v_log_f32_e32 v38, v38
	v_log_f32_e32 v39, v39
	v_exp_f32_e32 v40, v40
	v_exp_f32_e32 v61, v61
	v_log_f32_e32 v78, v59
	v_add_f32_e32 v59, 1.0, v60
	v_max_f32_e32 v60, v113, v113
	v_xor_b32_e32 v55, 0x80000000, v37
	v_xor_b32_e32 v57, 0x80000000, v38
	v_xor_b32_e32 v58, 0x80000000, v39
	v_add_f32_e32 v37, 1.0, v40
	v_max_f32_e32 v38, v103, v103
	v_max_f32_e32 v39, v87, v87
	v_max_f32_e32 v40, v104, v104
	v_max_f32_e32 v41, v88, v88
	v_max_f32_e32 v42, v105, v105
	v_max_f32_e32 v43, v89, v89
	v_max_f32_e32 v44, v106, v106
	v_max_f32_e32 v45, v90, v90
	v_max_f32_e32 v46, v107, v107
	v_max_f32_e32 v47, v91, v91
	v_max_f32_e32 v48, v108, v108
	v_max_f32_e32 v49, v92, v92
	v_max_f32_e32 v50, v109, v109
	v_max_f32_e32 v51, v93, v93
	v_log_f32_e32 v79, v59
	v_add_f32_e32 v59, 1.0, v61
	v_min_f32_e32 v60, 0x42c80000, v60
	v_max_f32_e32 v61, v97, v97
	v_min_f32_e32 v38, 0x42c80000, v38
	v_min_f32_e32 v39, 0x42c80000, v39
	v_min_f32_e32 v40, 0x42c80000, v40
	v_min_f32_e32 v41, 0x42c80000, v41
	v_min_f32_e32 v42, 0x42c80000, v42
	v_min_f32_e32 v43, 0x42c80000, v43
	v_min_f32_e32 v44, 0x42c80000, v44
	v_min_f32_e32 v45, 0x42c80000, v45
	v_min_f32_e32 v46, 0x42c80000, v46
	v_min_f32_e32 v47, 0x42c80000, v47
	v_min_f32_e32 v48, 0x42c80000, v48
	v_min_f32_e32 v49, 0x42c80000, v49
	v_min_f32_e32 v50, 0x42c80000, v50
	v_min_f32_e32 v51, 0x42c80000, v51
	v_exp_f32_e32 v60, v60
	v_min_f32_e32 v61, 0x42c80000, v61
	v_exp_f32_e32 v38, v38
	v_exp_f32_e32 v39, v39
	v_exp_f32_e32 v40, v40
	v_exp_f32_e32 v41, v41
	v_exp_f32_e32 v42, v42
	v_exp_f32_e32 v43, v43
	v_exp_f32_e32 v44, v44
	v_exp_f32_e32 v45, v45
	v_exp_f32_e32 v46, v46
	v_exp_f32_e32 v47, v47
	v_exp_f32_e32 v48, v48
	v_exp_f32_e32 v49, v49
	v_exp_f32_e32 v50, v50
	v_exp_f32_e32 v51, v51
	v_exp_f32_e32 v61, v61
	v_log_f32_e32 v80, v59
	v_add_f32_e32 v59, 1.0, v60
	v_add_f32_e32 v38, 1.0, v38
	v_add_f32_e32 v39, 1.0, v39
	v_add_f32_e32 v40, 1.0, v40
	v_add_f32_e32 v41, 1.0, v41
	v_add_f32_e32 v42, 1.0, v42
	v_add_f32_e32 v43, 1.0, v43
	v_add_f32_e32 v44, 1.0, v44
	v_add_f32_e32 v45, 1.0, v45
	v_add_f32_e32 v46, 1.0, v46
	v_add_f32_e32 v47, 1.0, v47
	v_add_f32_e32 v48, 1.0, v48
	v_add_f32_e32 v49, 1.0, v49
; __device__ __forceinline__ float ex2(float x) { return __builtin_amdgcn_exp2f(x); }
; __device__ __forceinline__ float lg2(float x) { return __builtin_amdgcn_logf(x); }
; __device__ __forceinline__ void sb_unit(int b, int h, int qb, const bf16_t* __restrict__ PROJ, bf16_t* OCAT, float* SSQO, ldsp shm, volatile LAS unsigned* FL) {
;     ...
;             for (int r = 0; r < 16; ++r) { l0[r] = -lg2(1.0f + ex2(fminf(z0[r], 100.f))); l1[r] = -lg2(1.0f + ex2(fminf(z1[r], 100.f))); }
;             if (diag) {
; #pragma unroll
;                 for (int r = 0; r < 16; ++r) { const int kk = kb0 + (r & 3) + 8 * (r >> 2); if (kk >= qabs) l0[r] = 0.f; if (kk + 32 >= qabs) l1[r] = 0.f; } }
; #pragma unroll
;             for (int r = 0; r < 16; ++r) { tot += l0[r] + l1[r]; z0[r] += l0[r]; z1[r] += l1[r]; }
	v_add_f32_e32 v50, 1.0, v50
	v_add_f32_e32 v51, 1.0, v51
	v_log_f32_e32 v81, v59
	v_add_f32_e32 v59, 1.0, v61
	v_log_f32_e32 v37, v37
	v_log_f32_e32 v38, v38
	v_log_f32_e32 v39, v39
	v_log_f32_e32 v40, v40
	v_log_f32_e32 v41, v41
	v_log_f32_e32 v42, v42
	v_log_f32_e32 v43, v43
	v_log_f32_e32 v44, v44
	v_log_f32_e32 v45, v45
	v_log_f32_e32 v46, v46
	v_log_f32_e32 v47, v47
	v_log_f32_e32 v48, v48
	v_log_f32_e32 v49, v49
	v_log_f32_e32 v50, v50
	v_log_f32_e32 v51, v51
	v_log_f32_e32 v114, v59
	v_add_u32_e32 v59, s33, v165
	v_add_u32_e32 v167, 0xc0, v59
	v_add_u32_e32 v168, 0xe0, v59
	v_add_u32_e32 v169, 0xc1, v59
	v_add_u32_e32 v170, 0xe1, v59
	v_add_u32_e32 v171, 0xc2, v59
	v_add_u32_e32 v172, 0xe2, v59
	v_add_u32_e32 v173, 0xc3, v59
	v_add_u32_e32 v174, 0xe3, v59
	v_add_u32_e32 v175, 0xc8, v59
	v_add_u32_e32 v176, 0xe8, v59
	v_add_u32_e32 v177, 0xc9, v59
	v_add_u32_e32 v178, 0xe9, v59
	v_add_u32_e32 v179, 0xca, v59
	v_add_u32_e32 v180, 0xea, v59
	v_add_u32_e32 v181, 0xcb, v59
	v_add_u32_e32 v182, 0xeb, v59
	v_add_u32_e32 v183, 0xd0, v59
	v_add_u32_e32 v184, 0xf0, v59
	v_add_u32_e32 v185, 0xd1, v59
	v_add_u32_e32 v186, 0xf1, v59
	v_add_u32_e32 v187, 0xd2, v59
	v_add_u32_e32 v188, 0xf2, v59
	v_add_u32_e32 v189, 0xd3, v59
	v_add_u32_e32 v190, 0xf3, v59
	v_add_u32_e32 v191, 0xd8, v59
	v_add_u32_e32 v192, 0xf8, v59
	v_add_u32_e32 v193, 0xd9, v59
	v_add_u32_e32 v194, 0xf9, v59
	v_add_u32_e32 v195, 0xda, v59
	v_add_u32_e32 v196, 0xfa, v59
	v_add_u32_e32 v197, 0xdb, v59
	v_add_u32_e32 v166, 0xfb, v59
	v_cmp_lt_i32_e64 s[44:45], v167, v163
	v_cmp_lt_i32_e64 s[6:7], v168, v163
	v_cmp_lt_i32_e64 s[68:69], v169, v163
	v_cmp_lt_i32_e64 s[0:1], v170, v163
	v_cmp_lt_i32_e64 s[72:73], v171, v163
	v_cmp_lt_i32_e64 s[40:41], v172, v163
	v_cmp_lt_i32_e64 s[76:77], v173, v163
	v_cmp_lt_i32_e64 s[42:43], v174, v163
	v_cmp_lt_i32_e64 s[78:79], v175, v163
	v_cmp_lt_i32_e64 s[48:49], v176, v163
	v_cmp_lt_i32_e64 s[80:81], v177, v163
	v_cmp_lt_i32_e64 s[50:51], v178, v163
	v_cmp_lt_i32_e64 s[82:83], v179, v163
	v_cmp_lt_i32_e64 s[52:53], v180, v163
	v_cmp_lt_i32_e64 s[84:85], v181, v163
	v_cmp_lt_i32_e64 s[54:55], v182, v163
	v_cmp_lt_i32_e64 s[88:89], v183, v163
	v_cmp_lt_i32_e64 s[58:59], v184, v163
	v_cmp_lt_i32_e64 s[90:91], v185, v163
	v_cmp_lt_i32_e64 s[60:61], v186, v163
	v_cmp_lt_i32_e64 s[92:93], v187, v163
	v_cmp_lt_i32_e64 s[62:63], v188, v163
	v_cmp_lt_i32_e64 s[94:95], v189, v163
	v_cmp_lt_i32_e64 s[64:65], v190, v163
	v_cmp_lt_i32_e64 s[96:97], v191, v163
	v_cmp_lt_i32_e64 s[66:67], v192, v163
	v_cmp_lt_i32_e64 s[4:5], v193, v163
	v_cmp_lt_i32_e64 s[70:71], v194, v163
	v_cmp_lt_i32_e32 vcc, v195, v163
	v_cmp_lt_i32_e64 s[74:75], v196, v163
	v_cmp_lt_i32_e64 s[86:87], v197, v163
	v_cmp_lt_i32_e64 s[56:57], v166, v163
	v_xor_b32_e32 v60, 0x80000000, v37
	v_xor_b32_e32 v59, 0x80000000, v38
	v_xor_b32_e32 v61, 0x80000000, v39
	v_xor_b32_e32 v62, 0x80000000, v40
	v_xor_b32_e32 v64, 0x80000000, v41
	v_xor_b32_e32 v63, 0x80000000, v42
	v_xor_b32_e32 v65, 0x80000000, v43
	v_xor_b32_e32 v66, 0x80000000, v44
	v_xor_b32_e32 v68, 0x80000000, v45
	v_xor_b32_e32 v67, 0x80000000, v46
	v_xor_b32_e32 v69, 0x80000000, v47
	v_xor_b32_e32 v70, 0x80000000, v48
	v_xor_b32_e32 v72, 0x80000000, v49
	v_xor_b32_e32 v71, 0x80000000, v50
	v_xor_b32_e32 v73, 0x80000000, v51
	v_xor_b32_e32 v74, 0x80000000, v74
	v_xor_b32_e32 v76, 0x80000000, v75
	v_xor_b32_e32 v75, 0x80000000, v77
	v_xor_b32_e32 v77, 0x80000000, v78
	v_xor_b32_e32 v78, 0x80000000, v79
	v_xor_b32_e32 v80, 0x80000000, v80
	v_xor_b32_e32 v79, 0x80000000, v81
	v_xor_b32_e32 v81, 0x80000000, v114
	s_cbranch_scc1 .LBB0_1058
	s_or_b64 vcc, s[86:87], vcc
	v_cndmask_b32_e32 v78, 0, v78, vcc
	s_or_b64 vcc, vcc, s[4:5]
	v_cndmask_b32_e32 v75, 0, v75, vcc
	s_or_b64 vcc, vcc, s[96:97]
	v_cndmask_b32_e32 v74, 0, v74, vcc
	s_or_b64 vcc, vcc, s[94:95]
	v_cndmask_b32_e32 v71, 0, v71, vcc
	s_or_b64 vcc, vcc, s[92:93]
	v_cndmask_b32_e32 v70, 0, v70, vcc
	s_or_b64 vcc, vcc, s[90:91]
	v_cndmask_b32_e32 v67, 0, v67, vcc
	s_or_b64 vcc, vcc, s[88:89]
	v_cndmask_b32_e32 v66, 0, v66, vcc
	s_or_b64 vcc, vcc, s[84:85]
	v_cndmask_b32_e32 v63, 0, v63, vcc
	s_or_b64 vcc, vcc, s[82:83]
	v_cndmask_b32_e32 v62, 0, v62, vcc
	s_or_b64 vcc, vcc, s[80:81]
	v_cndmask_b32_e32 v59, 0, v59, vcc
	s_or_b64 vcc, vcc, s[78:79]
	v_cndmask_b32_e32 v58, 0, v58, vcc
	s_or_b64 vcc, vcc, s[76:77]
	v_cndmask_b32_e32 v55, 0, v55, vcc
	s_or_b64 vcc, vcc, s[72:73]
	v_cndmask_b32_e32 v54, 0, v54, vcc
	s_or_b64 vcc, vcc, s[68:69]
	v_cndmask_b32_e32 v1, 0, v1, vcc
	s_or_b64 vcc, vcc, s[44:45]
	v_cndmask_b32_e32 v2, 0, v2, vcc
	s_or_b64 vcc, s[56:57], s[74:75]
	v_cndmask_b32_e32 v80, 0, v80, vcc
	s_or_b64 vcc, vcc, s[70:71]
	v_cndmask_b32_e32 v77, 0, v77, vcc
	s_or_b64 vcc, vcc, s[66:67]
	v_cndmask_b32_e32 v76, 0, v76, vcc
	s_or_b64 vcc, vcc, s[64:65]
	v_cndmask_b32_e32 v73, 0, v73, vcc
	s_or_b64 vcc, vcc, s[62:63]
	v_cndmask_b32_e32 v72, 0, v72, vcc
	s_or_b64 vcc, vcc, s[60:61]
	v_cndmask_b32_e32 v69, 0, v69, vcc
	s_or_b64 vcc, vcc, s[58:59]
	v_cndmask_b32_e32 v68, 0, v68, vcc
	s_or_b64 vcc, vcc, s[54:55]
	v_cndmask_b32_e32 v65, 0, v65, vcc
	s_or_b64 vcc, vcc, s[52:53]
	v_cndmask_b32_e32 v64, 0, v64, vcc
	s_or_b64 vcc, vcc, s[50:51]
	v_cndmask_b32_e32 v61, 0, v61, vcc
	s_or_b64 vcc, vcc, s[48:49]
	v_cndmask_b32_e32 v60, 0, v60, vcc
	s_or_b64 vcc, vcc, s[42:43]
	v_cndmask_b32_e32 v57, 0, v57, vcc
	s_or_b64 vcc, vcc, s[40:41]
	v_cndmask_b32_e32 v56, 0, v56, vcc
	s_or_b64 vcc, vcc, s[0:1]
	v_cndmask_b32_e32 v53, 0, v53, vcc
	s_or_b64 vcc, vcc, s[6:7]
	v_cndmask_b32_e64 v79, 0, v79, s[86:87]
	v_cndmask_b32_e32 v52, 0, v52, vcc
	v_cndmask_b32_e64 v81, 0, v81, s[56:57]

; #define LAS __attribute__((address_space(3)))
; __device__ __forceinline__ float ex2(float x) { return __builtin_amdgcn_exp2f(x); }
; __device__ __forceinline__ f32x16 mfma32(bf16x8 a, bf16x8 b, f32x16 c) { return __builtin_amdgcn_mfma_f32_32x32x16_bf16(a, b, c, 0, 0, 0); }
; #define MLA_WAITBAR() do { if (wid < 4) asm volatile("s_waitcnt vmcnt(6) lgkmcnt(0)\n\ts_barrier" ::: "memory"); else asm volatile("s_waitcnt vmcnt(4) lgkmcnt(0)\n\ts_barrier" ::: "memory"); } while (0)
; #define MLA_ISSUE(s) do { const int tk_ = (s) + 3 < NT - 1 ? (s) + 3 : NT - 1, tv_ = (s) + 2 < 0 ? 0 : ((s) + 2 < NT - 1 ? (s) + 2 : NT - 1); MLA_DMAK(tk_, ((s) + 3) & 3); MLA_DMAV(tv_, ((s) + 2) & 3); } while (0)
; #define PIN(x) asm volatile("" : "+v"(x))
; __device__ __forceinline__ void mla_unit(int b, int h, int qb, const bf16_t* __restrict__ Q, const bf16_t* __restrict__ KV, const bf16_t* __restrict__ PROJ, bf16_t* OCAT, float* SSQO, ldsp shm) {
;     ...
;     const LAS unsigned char* vp0 = shm + VOFF + ((lane >> 4) & 1) * 32 + (lane & 3) * 8 + (4 * hi + ((lane & 15) >> 2)) * 64;
;     const LAS unsigned char* kp0 = shm + hi * 1024 + r32 * 16;
;     float mhat = 0.f, l_reg = 0.f; f32x16 o[2]; o[0] = f32x16{}; o[1] = f32x16{}; f32x16 negm = f32x16{};
;     f32x16 pA0, pA1, pB0, pB1;
;     ...
;     MLA_WAITBAR();
;     MLA_ISSUE(0);
;     { const LAS unsigned char* kb = kp0; pA0 = f32x16{}; pA1 = f32x16{};
; #pragma unroll
;       for (int d0 = 0; d0 < 6; ++d0) { const bf16x8 k0 = *(const LAS bf16x8*)(kb + d0 * 2048), k1 = *(const LAS bf16x8*)(kb + d0 * 2048 + 512); pA0 = mfma32(k0, qr[d0], pA0); pA1 = mfma32(k1, qr[d0], pA1); }
;       mhat = rowmax(pA0, pA1);
; #pragma unroll
;       for (int r = 0; r < 16; ++r) { negm[r] = -mhat; pA0[r] = ex2(pA0[r] - mhat); pA1[r] = ex2(pA1[r] - mhat); } }
;     PIN(negm);
.LBB0_1145:
	s_mov_b64 s[10:11], 0x40000
	v_lshlrev_b32_e32 v6, 10, v184
	v_lshlrev_b32_e32 v7, 4, v183
	v_lshl_add_u64 v[4:5], v[4:5], 0, s[10:11]
	s_add_i32 m0, s26, 0x10000
	v_add3_u32 v188, 0, v6, v7
	global_load_lds_dwordx4 v[4:5], off
	ds_read_b128 v[4:7], v188
	ds_read_b128 v[10:13], v188 offset:512
	s_waitcnt vmcnt(0) lgkmcnt(0)
	v_mfma_f32_32x32x16_bf16 v[20:35], v[4:7], v[136:139], 0
	v_lshlrev_b32_e32 v9, 8, v184
	s_and_b32 s8, s2, 0x3fffffc0
	s_lshl_b32 s8, s8, 2
	s_add_i32 s51, s8, 0
	s_mov_b32 s8, s9
	s_mov_b32 s10, s9
	s_mov_b32 s11, s9
	v_mfma_f32_32x32x16_bf16 v[52:67], v[10:13], v[136:139], 0
	ds_read_b128 v[4:7], v188 offset:2048
	ds_read_b128 v[10:13], v188 offset:2560
	s_mov_b32 s12, s9
	s_mov_b32 s13, s9
	s_mov_b32 s14, s9
	s_mov_b32 s15, s9
	s_mov_b32 s16, s9
	s_mov_b32 s17, s9
	s_waitcnt lgkmcnt(1)
	v_mfma_f32_32x32x16_bf16 v[20:35], v[4:7], v[132:135], v[20:35]
	s_mov_b32 s18, s9
	s_mov_b32 s19, s9
	s_mov_b32 s20, s9
	s_mov_b32 s21, s9
	s_mov_b32 s22, s9
	s_mov_b32 s23, s9
	s_lshl_b32 s3, s3, 2
	s_waitcnt lgkmcnt(0)
	v_mfma_f32_32x32x16_bf16 v[52:67], v[10:13], v[132:135], v[52:67]
	ds_read_b128 v[4:7], v188 offset:4096
	ds_read_b128 v[10:13], v188 offset:4608
	s_ashr_i32 s2, s2, 7
	s_add_i32 s51, s51, 0x14000
	s_add_i32 s52, s2, s3
	s_mov_b32 s27, 2
	s_add_i32 s52, s52, 1
	s_or_b32 s2, s3, 3
	s_waitcnt lgkmcnt(1)
	v_mfma_f32_32x32x16_bf16 v[20:35], v[4:7], v[128:131], v[20:35]
	ds_read_b128 v[4:7], v188 offset:6144
	ds_read_b128 v[36:39], v188 offset:10752
	v_cmp_gt_u32_e64 s[36:37], 32, v182
	v_lshl_add_u32 v185, v183, 2, s51
	v_mov_b32_e32 v189, 0
	s_waitcnt lgkmcnt(2)
	v_mfma_f32_32x32x16_bf16 v[52:67], v[10:13], v[128:131], v[52:67]
	ds_read_b128 v[10:13], v188 offset:6656
	s_waitcnt lgkmcnt(2)
	v_mfma_f32_32x32x16_bf16 v[20:35], v[4:7], v[124:127], v[20:35]
	v_lshlrev_b32_e32 v4, 1, v1
	v_and_b32_e32 v4, 32, v4
	v_add3_u32 v8, 0, v4, v8
	v_lshlrev_b32_e32 v4, 4, v1
	v_and_b32_e32 v14, 0xc0, v4
	ds_read_b128 v[4:7], v188 offset:8192
	v_add3_u32 v186, v8, v9, v14
	s_waitcnt lgkmcnt(1)
	v_mfma_f32_32x32x16_bf16 v[52:67], v[10:13], v[124:127], v[52:67]
	ds_read_b128 v[8:11], v188 offset:8704
	s_waitcnt lgkmcnt(1)
	v_mfma_f32_32x32x16_bf16 v[20:35], v[4:7], v[120:123], v[20:35]
	ds_read_b128 v[4:7], v188 offset:10240
	s_waitcnt lgkmcnt(1)
	v_mfma_f32_32x32x16_bf16 v[52:67], v[8:11], v[120:123], v[52:67]
	s_waitcnt lgkmcnt(0)
	v_mfma_f32_32x32x16_bf16 v[20:35], v[4:7], v[116:119], v[20:35]
	v_mov_b64_e32 v[4:5], s[8:9]
	v_mov_b64_e32 v[18:19], s[22:23]
	v_mov_b64_e32 v[6:7], s[10:11]
	v_mov_b64_e32 v[8:9], s[12:13]
	v_mov_b64_e32 v[10:11], s[14:15]
	v_mov_b64_e32 v[12:13], s[16:17]
	v_mov_b64_e32 v[14:15], s[18:19]
	v_mfma_f32_32x32x16_bf16 v[52:67], v[36:39], v[116:119], v[52:67]
	s_nop 3
	v_max_f32_e32 v40, v21, v21
	v_max_f32_e32 v41, v20, v20
	v_max_f32_e32 v40, v41, v40
	v_mov_b64_e32 v[16:17], s[20:21]
	s_mov_b32 s14, 0x8000
	s_nop 2
	v_max3_f32 v36, v22, v23, v53
	v_max3_f32 v37, v40, v52, v54
	v_max3_f32 v37, v37, v55, v24
	v_max3_f32 v36, v36, v26, v27
	v_max3_f32 v37, v37, v25, v56
	v_max3_f32 v36, v36, v58, v59
	v_max3_f32 v37, v37, v57, v28
	v_max3_f32 v36, v36, v30, v31
	v_max3_f32 v37, v37, v29, v60
	v_max3_f32 v36, v36, v62, v63
	v_max3_f32 v37, v37, v61, v32
	v_max3_f32 v36, v36, v34, v35
	v_max3_f32 v37, v37, v33, v64
	v_max3_f32 v36, v36, v66, v67
	v_max3_f32 v36, v37, v65, v36
	v_mov_b32_e32 v37, v36
	s_nop 1
	v_permlane32_swap_b32_e32 v36, v37
	v_max_f32_e32 v37, v37, v37
	v_max_f32_e32 v36, v36, v36
	v_max_f32_e32 v187, v36, v37
	v_sub_f32_e32 v20, v20, v187
	v_exp_f32_e32 v68, v20
	v_sub_f32_e32 v20, v21, v187
	v_exp_f32_e32 v69, v20
	v_sub_f32_e32 v20, v22, v187
	v_exp_f32_e32 v70, v20
	v_sub_f32_e32 v20, v23, v187
	v_exp_f32_e32 v71, v20
	v_sub_f32_e32 v20, v24, v187
	v_exp_f32_e32 v72, v20
	v_sub_f32_e32 v20, v25, v187
	v_exp_f32_e32 v73, v20
	v_sub_f32_e32 v20, v26, v187
	v_exp_f32_e32 v74, v20
	v_sub_f32_e32 v20, v27, v187
	v_exp_f32_e32 v75, v20
	v_sub_f32_e32 v20, v28, v187
	v_exp_f32_e32 v76, v20
	v_sub_f32_e32 v20, v29, v187
	v_exp_f32_e32 v77, v20
	v_sub_f32_e32 v20, v30, v187
	v_exp_f32_e32 v78, v20
	v_sub_f32_e32 v20, v31, v187
	v_exp_f32_e32 v79, v20
	v_sub_f32_e32 v20, v32, v187
	v_exp_f32_e32 v80, v20
	v_sub_f32_e32 v20, v33, v187
	v_exp_f32_e32 v81, v20
	v_sub_f32_e32 v20, v34, v187
	v_sub_f32_e32 v52, v52, v187
	v_sub_f32_e32 v53, v53, v187
	v_sub_f32_e32 v54, v54, v187
	v_sub_f32_e32 v55, v55, v187
	v_sub_f32_e32 v56, v56, v187
	v_sub_f32_e32 v57, v57, v187
	v_sub_f32_e32 v58, v58, v187
	v_sub_f32_e32 v59, v59, v187
	v_sub_f32_e32 v60, v60, v187
	v_sub_f32_e32 v61, v61, v187
	v_sub_f32_e32 v62, v62, v187
	v_sub_f32_e32 v63, v63, v187
	v_sub_f32_e32 v64, v64, v187
	v_sub_f32_e32 v65, v65, v187
	v_sub_f32_e32 v66, v66, v187
	v_sub_f32_e32 v67, v67, v187
	v_exp_f32_e32 v82, v20
	v_sub_f32_e32 v20, v35, v187
	v_exp_f32_e32 v52, v52
	v_exp_f32_e32 v53, v53
	v_exp_f32_e32 v54, v54
	v_exp_f32_e32 v55, v55
	v_exp_f32_e32 v56, v56
	v_exp_f32_e32 v57, v57
	v_exp_f32_e32 v58, v58
	v_exp_f32_e32 v59, v59
	v_exp_f32_e32 v83, v20
	v_xor_b32_e32 v36, 0x80000000, v187
	v_mov_b64_e32 v[34:35], v[18:19]
	v_mov_b32_e32 v37, v36
	v_mov_b32_e32 v38, v36
	v_mov_b32_e32 v39, v36
	v_mov_b32_e32 v40, v36
	v_mov_b32_e32 v41, v36
	v_mov_b32_e32 v42, v36
	v_mov_b32_e32 v43, v36
	v_mov_b32_e32 v44, v36
	v_mov_b32_e32 v45, v36
	v_mov_b32_e32 v46, v36
	v_mov_b32_e32 v47, v36
	v_mov_b32_e32 v48, v36
	v_mov_b32_e32 v49, v36
	v_mov_b32_e32 v50, v36
	v_mov_b32_e32 v51, v36
	v_mov_b64_e32 v[32:33], v[16:17]
	v_mov_b64_e32 v[30:31], v[14:15]
	v_mov_b64_e32 v[28:29], v[12:13]
	v_mov_b64_e32 v[26:27], v[10:11]
	v_mov_b64_e32 v[24:25], v[8:9]
	v_mov_b64_e32 v[22:23], v[6:7]
	v_mov_b64_e32 v[20:21], v[4:5]
	s_mov_b64 s[10:11], -1
	s_and_b64 vcc, exec, s[40:41]
	s_cbranch_vccz .LBB0_1147

.LBB0_1149:
	s_add_i32 s19, s27, -1
	s_and_b32 s18, s19, 3
	s_mul_i32 s20, s18, 0x3000
	v_add_u32_e32 v156, s20, v188
	s_and_b32 s17, s14, 0x6000
	v_add_u32_e32 v157, s17, v186
	ds_read_b128 v[84:87], v156
	ds_read_b128 v[190:193], v156 offset:512
	ds_read_b128 v[194:197], v156 offset:2048
	ds_read_b128 v[198:201], v156 offset:2560
	v_exp_f32_e32 v60, v60
	v_exp_f32_e32 v61, v61
	v_exp_f32_e32 v62, v62
	v_exp_f32_e32 v63, v63
	v_exp_f32_e32 v64, v64
	v_exp_f32_e32 v65, v65
	v_exp_f32_e32 v66, v66
	v_exp_f32_e32 v67, v67
	s_setprio 1
	s_waitcnt lgkmcnt(0)
	v_mfma_f32_32x32x16_bf16 v[100:115], v[84:87], v[136:139], v[36:51]
	v_add_f32_e32 v88, v68, v69
	ds_read_b128 v[202:205], v156 offset:4096
	ds_read_b64_tr_b16 v[172:173], v157 offset:49152
	ds_read_b64_tr_b16 v[174:175], v157 offset:49664
	v_add_f32_e32 v84, v70, v88
	v_add_f32_e32 v84, v71, v84
	v_add_f32_e32 v84, v72, v84
	v_add_f32_e32 v144, v73, v84
	v_cvt_pk_bf16_f32 v140, v68, v69
	v_cvt_pk_bf16_f32 v141, v70, v71
	v_mfma_f32_32x32x16_bf16 v[84:99], v[190:193], v[136:139], v[36:51]
	ds_read_b128 v[190:193], v156 offset:4608
	ds_read_b64_tr_b16 v[68:69], v157 offset:53248
	ds_read_b64_tr_b16 v[70:71], v157 offset:53760
	v_add_f32_e32 v142, v74, v144
	v_add_f32_e32 v142, v75, v142
	v_add_f32_e32 v142, v76, v142
	v_add_f32_e32 v144, v77, v142
	v_cvt_pk_bf16_f32 v142, v72, v73
	v_cvt_pk_bf16_f32 v143, v74, v75
	v_mfma_f32_32x32x16_bf16 v[100:115], v[194:197], v[132:135], v[100:115]
	ds_read_b128 v[194:197], v156 offset:6144
	ds_read_b64_tr_b16 v[72:73], v157 offset:50176
	ds_read_b64_tr_b16 v[74:75], v157 offset:50688
	v_add_f32_e32 v144, v78, v144
	v_add_f32_e32 v144, v79, v144
	v_add_f32_e32 v144, v80, v144
	v_add_f32_e32 v148, v81, v144
	v_cvt_pk_bf16_f32 v144, v76, v77
	v_cvt_pk_bf16_f32 v145, v78, v79
	v_mfma_f32_32x32x16_bf16 v[84:99], v[198:201], v[132:135], v[84:99]
	ds_read_b128 v[198:201], v156 offset:6656
	ds_read_b64_tr_b16 v[76:77], v157 offset:54272
	ds_read_b64_tr_b16 v[78:79], v157 offset:54784
	v_add_f32_e32 v146, v82, v148
	v_add_f32_e32 v146, v83, v146
	v_add_f32_e32 v146, v52, v146
	v_add_f32_e32 v148, v53, v146
	v_cvt_pk_bf16_f32 v146, v80, v81
	v_cvt_pk_bf16_f32 v147, v82, v83
	s_waitcnt lgkmcnt(0)
	v_mfma_f32_32x32x16_bf16 v[100:115], v[202:205], v[128:131], v[100:115]
	ds_read_b128 v[202:205], v156 offset:8192
	ds_read_b64_tr_b16 v[80:81], v157 offset:51200
	ds_read_b64_tr_b16 v[82:83], v157 offset:51712
	v_add_f32_e32 v148, v54, v148
	v_add_f32_e32 v148, v55, v148
	v_add_f32_e32 v148, v56, v148
	v_add_f32_e32 v152, v57, v148
	v_cvt_pk_bf16_f32 v148, v52, v53
	v_cvt_pk_bf16_f32 v149, v54, v55
	v_mfma_f32_32x32x16_bf16 v[84:99], v[190:193], v[128:131], v[84:99]
	ds_read_b128 v[190:193], v156 offset:8704
	ds_read_b64_tr_b16 v[52:53], v157 offset:55296
	ds_read_b64_tr_b16 v[54:55], v157 offset:55808
	v_add_f32_e32 v150, v58, v152
	v_add_f32_e32 v150, v59, v150
	v_add_f32_e32 v150, v60, v150
	v_add_f32_e32 v152, v61, v150
	v_cvt_pk_bf16_f32 v150, v56, v57
	v_cvt_pk_bf16_f32 v151, v58, v59
	v_mfma_f32_32x32x16_bf16 v[100:115], v[194:197], v[124:127], v[100:115]
	ds_read_b128 v[194:197], v156 offset:10240
	ds_read_b64_tr_b16 v[56:57], v157 offset:52224
	ds_read_b64_tr_b16 v[58:59], v157 offset:52736
	v_add_f32_e32 v152, v62, v152
	v_add_f32_e32 v152, v63, v152
	v_add_f32_e32 v152, v64, v152
	v_add_f32_e32 v160, v65, v152
	v_cvt_pk_bf16_f32 v152, v60, v61
	v_cvt_pk_bf16_f32 v153, v62, v63
	v_mfma_f32_32x32x16_bf16 v[84:99], v[198:201], v[124:127], v[84:99]
	ds_read_b128 v[198:201], v156 offset:10752
	ds_read_b64_tr_b16 v[60:61], v157 offset:56320
	ds_read_b64_tr_b16 v[62:63], v157 offset:56832
	v_add_f32_e32 v154, v66, v160
	v_add_f32_e32 v154, v67, v154
	v_add_f32_e32 v156, 0, v154
	v_cvt_pk_bf16_f32 v154, v64, v65
	v_cvt_pk_bf16_f32 v155, v66, v67
	s_waitcnt lgkmcnt(0)
	v_mfma_f32_32x32x16_bf16 v[100:115], v[202:205], v[120:123], v[100:115]
	s_add_i32 s16, s27, 2
	s_min_i32 s8, s16, s2
	s_lshl_b64 s[10:11], s[8:9], 17
	v_lshl_add_u64 v[202:203], v[176:177], 0, s[10:11]
	s_and_b32 s10, s16, 3
	s_mulk_i32 s10, 0x3000
	s_add_i32 s10, s26, s10
	s_mov_b32 m0, s10
	s_nop 0
	global_load_lds_dwordx4 v[202:203], off
	v_mfma_f32_32x32x16_bf16 v[84:99], v[190:193], v[120:123], v[84:99]
	s_and_b64 vcc, exec, s[38:39]
	s_cbranch_vccnz .Lmla_rope1
	s_lshl_b64 s[12:13], s[8:9], 18
	v_lshl_add_u64 v[202:203], v[180:181], 0, s[12:13]
	s_add_i32 m0, s10, 0x2000
	s_nop 0
	global_load_lds_dwordx4 v[202:203], off

.LBB0_1153:
	v_mfma_f32_32x32x16_bf16 v[4:19], v[140:143], v[172:175], v[4:19]
	v_exp_f32_e32 v100, v100
	v_exp_f32_e32 v101, v101
	v_exp_f32_e32 v102, v102
	v_exp_f32_e32 v103, v103
	v_mfma_f32_32x32x16_bf16 v[20:35], v[140:143], v[68:71], v[20:35]
	v_exp_f32_e32 v104, v104
	v_exp_f32_e32 v105, v105
	v_exp_f32_e32 v106, v106
	v_exp_f32_e32 v107, v107
	v_mfma_f32_32x32x16_bf16 v[4:19], v[144:147], v[72:75], v[4:19]
	v_exp_f32_e32 v108, v108
	v_exp_f32_e32 v109, v109
	v_exp_f32_e32 v110, v110
	v_exp_f32_e32 v111, v111
	v_mfma_f32_32x32x16_bf16 v[20:35], v[144:147], v[76:79], v[20:35]
	v_exp_f32_e32 v112, v112
	v_exp_f32_e32 v113, v113
	v_exp_f32_e32 v114, v114
	v_exp_f32_e32 v115, v115
	v_mfma_f32_32x32x16_bf16 v[4:19], v[148:151], v[80:83], v[4:19]
	v_exp_f32_e32 v84, v84
	v_exp_f32_e32 v85, v85
	v_exp_f32_e32 v86, v86
	v_exp_f32_e32 v87, v87
	v_mfma_f32_32x32x16_bf16 v[20:35], v[148:151], v[52:55], v[20:35]
	v_exp_f32_e32 v88, v88
	v_exp_f32_e32 v89, v89
	v_exp_f32_e32 v90, v90
	v_exp_f32_e32 v91, v91
	v_mfma_f32_32x32x16_bf16 v[4:19], v[152:155], v[56:59], v[4:19]
	v_mfma_f32_32x32x16_bf16 v[20:35], v[152:155], v[60:63], v[20:35]
	s_andn2_b64 vcc, exec, s[10:11]
	s_cbranch_vccnz .LBB0_1155
	s_waitcnt lgkmcnt(0)
	v_add_u32_e32 v64, s51, v2
	ds_read_b128 v[52:55], v64 offset:96
	ds_read_b128 v[56:59], v64 offset:64
	ds_read_b128 v[60:63], v64 offset:32
	ds_read_b128 v[64:67], v64
	s_waitcnt lgkmcnt(0)
	v_pk_mul_f32 v[16:17], v[16:17], v[52:53]
	v_pk_mul_f32 v[12:13], v[12:13], v[56:57]
	v_pk_mul_f32 v[8:9], v[8:9], v[60:61]
	v_pk_mul_f32 v[18:19], v[18:19], v[54:55]
	v_pk_mul_f32 v[14:15], v[14:15], v[58:59]
	v_pk_mul_f32 v[10:11], v[10:11], v[62:63]
	v_pk_mul_f32 v[6:7], v[6:7], v[66:67]
	v_pk_mul_f32 v[4:5], v[4:5], v[64:65]
	v_pk_mul_f32 v[32:33], v[32:33], v[52:53]
	v_pk_mul_f32 v[28:29], v[28:29], v[56:57]
	v_pk_mul_f32 v[24:25], v[24:25], v[60:61]
	v_pk_mul_f32 v[34:35], v[34:35], v[54:55]
	v_pk_mul_f32 v[30:31], v[30:31], v[58:59]
	v_pk_mul_f32 v[26:27], v[26:27], v[62:63]
	v_pk_mul_f32 v[22:23], v[22:23], v[66:67]
	v_pk_mul_f32 v[20:21], v[20:21], v[64:65]

.LBB0_1159:
	s_and_b32 s12, s27, 3
	s_mulk_i32 s12, 0x3000
	v_add_u32_e32 v140, s12, v188
	v_lshl_add_u32 v141, s18, 13, v186
	ds_read_b128 v[52:55], v140
	ds_read_b128 v[190:193], v140 offset:512
	ds_read_b128 v[194:197], v140 offset:2048
	ds_read_b128 v[198:201], v140 offset:2560
	v_exp_f32_e32 v92, v92
	v_exp_f32_e32 v93, v93
	v_exp_f32_e32 v94, v94
	v_exp_f32_e32 v95, v95
	v_exp_f32_e32 v96, v96
	v_exp_f32_e32 v97, v97
	v_exp_f32_e32 v98, v98
	v_exp_f32_e32 v99, v99
	s_setprio 1
	s_waitcnt lgkmcnt(0)
	v_mfma_f32_32x32x16_bf16 v[68:83], v[52:55], v[136:139], v[36:51]
	v_add_f32_e32 v56, v100, v101
	ds_read_b128 v[202:205], v140 offset:4096
	ds_read_b64_tr_b16 v[172:173], v141 offset:49152
	ds_read_b64_tr_b16 v[174:175], v141 offset:49664
	v_add_f32_e32 v52, v102, v56
	v_add_f32_e32 v52, v103, v52
	v_add_f32_e32 v52, v104, v52
	v_add_f32_e32 v144, v105, v52
	v_cvt_pk_bf16_f32 v156, v100, v101
	v_cvt_pk_bf16_f32 v157, v102, v103
	v_mfma_f32_32x32x16_bf16 v[52:67], v[190:193], v[136:139], v[36:51]
	ds_read_b128 v[190:193], v140 offset:4608
	ds_read_b64_tr_b16 v[100:101], v141 offset:53248
	ds_read_b64_tr_b16 v[102:103], v141 offset:53760
	v_add_f32_e32 v144, v106, v144
	v_add_f32_e32 v144, v107, v144
	v_add_f32_e32 v144, v108, v144
	v_add_f32_e32 v144, v109, v144
	v_cvt_pk_bf16_f32 v158, v104, v105
	v_cvt_pk_bf16_f32 v159, v106, v107
	v_mfma_f32_32x32x16_bf16 v[68:83], v[194:197], v[132:135], v[68:83]
	ds_read_b128 v[194:197], v140 offset:6144
	ds_read_b64_tr_b16 v[104:105], v141 offset:50176
	ds_read_b64_tr_b16 v[106:107], v141 offset:50688
	v_add_f32_e32 v144, v110, v144
	v_add_f32_e32 v144, v111, v144
	v_add_f32_e32 v144, v112, v144
	v_add_f32_e32 v144, v113, v144
	v_cvt_pk_bf16_f32 v160, v108, v109
	v_cvt_pk_bf16_f32 v161, v110, v111
	v_mfma_f32_32x32x16_bf16 v[52:67], v[198:201], v[132:135], v[52:67]
	ds_read_b128 v[198:201], v140 offset:6656
	ds_read_b64_tr_b16 v[108:109], v141 offset:54272
	ds_read_b64_tr_b16 v[110:111], v141 offset:54784
	v_add_f32_e32 v144, v114, v144
	v_add_f32_e32 v144, v115, v144
	v_add_f32_e32 v144, v84, v144
	v_add_f32_e32 v144, v85, v144
	v_cvt_pk_bf16_f32 v162, v112, v113
	v_cvt_pk_bf16_f32 v163, v114, v115
	s_waitcnt lgkmcnt(0)
	v_mfma_f32_32x32x16_bf16 v[68:83], v[202:205], v[128:131], v[68:83]
	ds_read_b128 v[202:205], v140 offset:8192
	ds_read_b64_tr_b16 v[112:113], v141 offset:51200
	ds_read_b64_tr_b16 v[114:115], v141 offset:51712
	v_add_f32_e32 v144, v86, v144
	v_add_f32_e32 v144, v87, v144
	v_add_f32_e32 v144, v88, v144
	v_add_f32_e32 v144, v89, v144
	v_cvt_pk_bf16_f32 v164, v84, v85
	v_cvt_pk_bf16_f32 v165, v86, v87
	v_mfma_f32_32x32x16_bf16 v[52:67], v[190:193], v[128:131], v[52:67]
	ds_read_b128 v[190:193], v140 offset:8704
	ds_read_b64_tr_b16 v[84:85], v141 offset:55296
	ds_read_b64_tr_b16 v[86:87], v141 offset:55808
	v_add_f32_e32 v144, v90, v144
	v_add_f32_e32 v144, v91, v144
	v_add_f32_e32 v144, v92, v144
	v_add_f32_e32 v144, v93, v144
	v_cvt_pk_bf16_f32 v166, v88, v89
	v_cvt_pk_bf16_f32 v167, v90, v91
	v_mfma_f32_32x32x16_bf16 v[68:83], v[194:197], v[124:127], v[68:83]
	ds_read_b128 v[194:197], v140 offset:10240
	ds_read_b64_tr_b16 v[88:89], v141 offset:52224
	ds_read_b64_tr_b16 v[90:91], v141 offset:52736
	v_add_f32_e32 v144, v94, v144
	v_add_f32_e32 v144, v95, v144
	v_add_f32_e32 v144, v96, v144
	v_add_f32_e32 v144, v97, v144
	v_cvt_pk_bf16_f32 v168, v92, v93
	v_cvt_pk_bf16_f32 v169, v94, v95
	v_mfma_f32_32x32x16_bf16 v[52:67], v[198:201], v[124:127], v[52:67]
	ds_read_b128 v[198:201], v140 offset:10752
	ds_read_b64_tr_b16 v[92:93], v141 offset:56320
	ds_read_b64_tr_b16 v[94:95], v141 offset:56832
	v_add_f32_e32 v140, v98, v144
	v_add_f32_e32 v140, v99, v140
	v_add_f32_e32 v140, 0, v140
	v_cvt_pk_bf16_f32 v170, v96, v97
	v_cvt_pk_bf16_f32 v171, v98, v99
	s_waitcnt lgkmcnt(0)
	v_mfma_f32_32x32x16_bf16 v[68:83], v[202:205], v[120:123], v[68:83]
	s_add_i32 s8, s27, 3
	s_min_i32 s8, s8, s2
	s_lshl_b64 s[10:11], s[8:9], 17
	v_lshl_add_u64 v[202:203], v[176:177], 0, s[10:11]
	s_add_i32 s10, s26, s20
	s_mov_b32 m0, s10
	s_nop 0
	global_load_lds_dwordx4 v[202:203], off
	v_mfma_f32_32x32x16_bf16 v[52:67], v[190:193], v[120:123], v[52:67]
	s_and_b64 vcc, exec, s[38:39]
	s_cbranch_vccnz .Lmla_rope2
	s_lshl_b64 s[12:13], s[8:9], 18
	v_lshl_add_u64 v[202:203], v[180:181], 0, s[12:13]
	s_add_i32 m0, s10, 0x2000
	s_nop 0
	global_load_lds_dwordx4 v[202:203], off

.LBB0_1163:
	v_mfma_f32_32x32x16_bf16 v[4:19], v[156:159], v[172:175], v[4:19]
	v_exp_f32_e32 v68, v68
	v_exp_f32_e32 v69, v69
	v_exp_f32_e32 v70, v70
	v_exp_f32_e32 v71, v71
	v_mfma_f32_32x32x16_bf16 v[20:35], v[156:159], v[100:103], v[20:35]
	v_exp_f32_e32 v72, v72
	v_exp_f32_e32 v73, v73
	v_exp_f32_e32 v74, v74
	v_exp_f32_e32 v75, v75
	v_mfma_f32_32x32x16_bf16 v[4:19], v[160:163], v[104:107], v[4:19]
	v_exp_f32_e32 v76, v76
	v_exp_f32_e32 v77, v77
	v_exp_f32_e32 v78, v78
	v_exp_f32_e32 v79, v79
	v_mfma_f32_32x32x16_bf16 v[20:35], v[160:163], v[108:111], v[20:35]
	v_exp_f32_e32 v80, v80
	v_exp_f32_e32 v81, v81
	v_exp_f32_e32 v82, v82
	v_exp_f32_e32 v83, v83
	v_mfma_f32_32x32x16_bf16 v[4:19], v[164:167], v[112:115], v[4:19]
	v_exp_f32_e32 v52, v52
	v_exp_f32_e32 v53, v53
	v_exp_f32_e32 v54, v54
	v_exp_f32_e32 v55, v55
	v_mfma_f32_32x32x16_bf16 v[20:35], v[164:167], v[84:87], v[20:35]
	v_exp_f32_e32 v56, v56
	v_exp_f32_e32 v57, v57
	v_exp_f32_e32 v58, v58
	v_exp_f32_e32 v59, v59
	v_mfma_f32_32x32x16_bf16 v[4:19], v[168:171], v[88:91], v[4:19]
	v_mfma_f32_32x32x16_bf16 v[20:35], v[168:171], v[92:95], v[20:35]
	s_andn2_b64 vcc, exec, s[10:11]
	s_cbranch_vccnz .LBB0_1165
	s_waitcnt lgkmcnt(0)
	v_add_u32_e32 v96, s51, v2
	ds_read_b128 v[84:87], v96 offset:96
	ds_read_b128 v[88:91], v96 offset:64
	ds_read_b128 v[92:95], v96 offset:32
	ds_read_b128 v[96:99], v96
	s_waitcnt lgkmcnt(0)
	v_pk_mul_f32 v[16:17], v[16:17], v[84:85]
	v_pk_mul_f32 v[12:13], v[12:13], v[88:89]
	v_pk_mul_f32 v[8:9], v[8:9], v[92:93]
	v_pk_mul_f32 v[18:19], v[18:19], v[86:87]
	v_pk_mul_f32 v[14:15], v[14:15], v[90:91]
	v_pk_mul_f32 v[10:11], v[10:11], v[94:95]
	v_pk_mul_f32 v[6:7], v[6:7], v[98:99]
	v_pk_mul_f32 v[4:5], v[4:5], v[96:97]
	v_pk_mul_f32 v[32:33], v[32:33], v[84:85]
	v_pk_mul_f32 v[28:29], v[28:29], v[88:89]
	v_pk_mul_f32 v[24:25], v[24:25], v[92:93]
	v_pk_mul_f32 v[34:35], v[34:35], v[86:87]
	v_pk_mul_f32 v[30:31], v[30:31], v[90:91]
	v_pk_mul_f32 v[26:27], v[26:27], v[94:95]
	v_pk_mul_f32 v[22:23], v[22:23], v[98:99]
	v_pk_mul_f32 v[20:21], v[20:21], v[96:97]

; __device__ __forceinline__ void mla_unit(int b, int h, int qb, const bf16_t* __restrict__ Q, const bf16_t* __restrict__ KV, const bf16_t* __restrict__ PROJ, bf16_t* OCAT, float* SSQO, ldsp shm) {
;     ...
;     STEP(pB0, pB1, pA0, pA1, t);
.LBB0_1179:
	s_and_b32 s10, s12, 3
	s_mulk_i32 s10, 0x3000
	v_add_u32_e32 v156, s10, v188
	s_and_b32 s10, s14, 0x6000
	v_add_u32_e32 v157, s10, v186
	ds_read_b128 v[100:103], v156
	ds_read_b128 v[104:107], v156 offset:512
	ds_read_b128 v[108:111], v156 offset:2048
	ds_read_b128 v[112:115], v156 offset:2560
	v_exp_f32_e32 v60, v60
	v_exp_f32_e32 v61, v61
	v_exp_f32_e32 v62, v62
	v_exp_f32_e32 v63, v63
	v_exp_f32_e32 v64, v64
	v_exp_f32_e32 v65, v65
	v_exp_f32_e32 v66, v66
	v_exp_f32_e32 v67, v67
	s_add_i32 s3, s17, 0
	s_lshl_b32 s8, s2, 17
	s_add_i32 s3, s3, s34
	v_lshl_add_u64 v[84:85], v[176:177], 0, s[8:9]
	s_mov_b32 m0, s3
	s_and_b64 vcc, exec, s[38:39]
	global_load_lds_dwordx4 v[84:85], off
	s_cbranch_vccnz .LBB0_1181
	s_lshl_b32 s10, s2, 18
	s_mov_b32 s11, s9
	v_lshl_add_u64 v[84:85], v[180:181], 0, s[10:11]
	s_add_i32 m0, s3, 0x2000
	s_nop 0
	global_load_lds_dwordx4 v[84:85], off
